# speedup vs baseline: 1.0065x; 1.0065x over previous
_Z6k_prepPKfS0_S0_S0_S0_S0_S0_S0_S0_S0_S0_S0_S0_PDv8_DF16_S2_S2_PfS0_:
	s_add_i32 s4, s2, 0x360
	s_add_i32 s5, s2, 0xfffffef8
	s_cmpk_lt_u32 s2, 0x108
	s_cselect_b32 s4, s4, s5
	s_add_i32 s5, s2, 0x468
	s_cmpk_lt_u32 s2, 0x100
	s_cselect_b32 s2, s5, s4
	s_cmpk_lt_u32 s2, 0x468
	s_mov_b64 s[4:5], -1
	s_cbranch_scc1 .LBB0_3
	s_andn2_b64 vcc, exec, s[4:5]
	s_cbranch_vccz .LBB0_46
